# attention: LDS-DMA issue interleaved between the first PV MFMAs instead of a block between QK and PV
# baseline (speedup 1.0000x reference)
.LBB0_1344:
	ds_read_b128 v[230:233], v203 offset:24576
	ds_read_b128 v[236:239], v203 offset:36864
	ds_read_b128 v[240:243], v204 offset:24576
	ds_read_b128 v[244:247], v204 offset:36864
	ds_read_b128 v[66:69], v201 offset:36864
	ds_read_b128 v[70:73], v201 offset:24576
	ds_read_b128 v[212:215], v202 offset:24576
	ds_read_b128 v[216:219], v202 offset:36864
	v_add_f32_e32 v168, 0, v169
	v_add_f32_e32 v168, v191, v168
	v_add_f32_e32 v168, v170, v168
	s_waitcnt lgkmcnt(2)
	v_mfma_f32_32x32x16_bf16 v[82:97], v[70:73], v[128:131], 0
	v_add_f32_e32 v168, v192, v168
	v_add_f32_e32 v168, v190, v168
	v_add_f32_e32 v168, v193, v168
	v_add_f32_e32 v168, v171, v168
	v_add_f32_e32 v168, v189, v168
	v_add_f32_e32 v168, v173, v168
	v_add_f32_e32 v168, v175, v168
	v_mfma_f32_32x32x16_bf16 v[66:81], v[66:69], v[128:131], 0
	v_add_f32_e32 v168, v174, v168
	v_add_f32_e32 v168, v188, v168
	v_exp_f32_e32 v162, v162
	v_add_f32_e32 v168, v164, v168
	v_exp_f32_e32 v163, v163
	v_add_f32_e32 v168, v166, v168
	v_exp_f32_e32 v160, v160
	v_mfma_f32_32x32x16_bf16 v[82:97], v[230:233], v[124:127], v[82:97]
	v_add_f32_e32 v168, v165, v168
	v_exp_f32_e32 v161, v161
	v_add_f32_e32 v168, v167, v168
	v_exp_f32_e32 v156, v156
	v_add_f32_e32 v168, v162, v168
	v_exp_f32_e32 v157, v157
	v_add_f32_e32 v168, v163, v168
	v_mfma_f32_32x32x16_bf16 v[66:81], v[236:239], v[124:127], v[66:81]
	ds_read_b128 v[230:233], v201 offset:24704
	ds_read_b128 v[236:239], v201 offset:36992
	v_exp_f32_e32 v152, v152
	v_add_f32_e32 v168, v160, v168
	v_exp_f32_e32 v153, v153
	v_add_f32_e32 v168, v161, v168
	v_exp_f32_e32 v150, v150
	v_add_f32_e32 v168, v156, v168
	v_mfma_f32_32x32x16_bf16 v[82:97], v[240:243], v[120:123], v[82:97]
	v_exp_f32_e32 v151, v151
	v_add_f32_e32 v168, v157, v168
	v_exp_f32_e32 v158, v158
	v_add_f32_e32 v168, v152, v168
	v_exp_f32_e32 v159, v159
	v_add_f32_e32 v168, v153, v168
	v_exp_f32_e32 v154, v154
	v_mfma_f32_32x32x16_bf16 v[66:81], v[244:247], v[120:123], v[66:81]
	ds_read_b128 v[240:243], v203 offset:24704
	ds_read_b128 v[244:247], v203 offset:36992
	v_add_f32_e32 v168, v150, v168
	v_exp_f32_e32 v155, v155
	v_add_f32_e32 v168, v151, v168
	v_exp_f32_e32 v148, v148
	v_add_f32_e32 v168, v158, v168
	v_exp_f32_e32 v149, v149
	s_waitcnt lgkmcnt(5)
	v_mfma_f32_32x32x16_bf16 v[82:97], v[212:215], v[116:119], v[82:97]
	v_add_f32_e32 v168, v159, v168
	v_add_f32_e32 v168, v154, v168
	v_add_f32_e32 v168, v155, v168
	v_add_f32_e32 v168, v148, v168
	s_waitcnt lgkmcnt(4)
	v_mfma_f32_32x32x16_bf16 v[66:81], v[216:219], v[116:119], v[66:81]
	ds_read_b128 v[212:215], v204 offset:24704
	ds_read_b128 v[216:219], v204 offset:36992
	s_waitcnt lgkmcnt(5)
	v_mfma_f32_32x32x16_bf16 v[82:97], v[230:233], v[112:115], v[82:97]
	s_waitcnt lgkmcnt(4)
	v_mfma_f32_32x32x16_bf16 v[66:81], v[236:239], v[112:115], v[66:81]
	ds_read_b128 v[230:233], v202 offset:24704
	ds_read_b128 v[236:239], v202 offset:36992
	s_waitcnt lgkmcnt(5)
	v_mfma_f32_32x32x16_bf16 v[82:97], v[240:243], v[108:111], v[82:97]
	s_waitcnt lgkmcnt(4)
	v_mfma_f32_32x32x16_bf16 v[66:81], v[244:247], v[108:111], v[66:81]
	ds_read_b128 v[240:243], v201 offset:24832
	ds_read_b128 v[244:247], v201 offset:37120
	s_waitcnt lgkmcnt(5)
	v_mfma_f32_32x32x16_bf16 v[82:97], v[212:215], v[104:107], v[82:97]
	s_waitcnt lgkmcnt(4)
	v_mfma_f32_32x32x16_bf16 v[66:81], v[216:219], v[104:107], v[66:81]
	ds_read_b128 v[212:215], v203 offset:24832
	ds_read_b128 v[216:219], v203 offset:37120
	s_waitcnt lgkmcnt(5)
	v_mfma_f32_32x32x16_bf16 v[82:97], v[230:233], v[100:103], v[82:97]
	s_waitcnt lgkmcnt(4)
	v_mfma_f32_32x32x16_bf16 v[66:81], v[236:239], v[100:103], v[66:81]
	ds_read_b128 v[230:233], v204 offset:24832
	ds_read_b128 v[236:239], v204 offset:37120
	s_waitcnt lgkmcnt(5)
	v_mfma_f32_32x32x16_bf16 v[82:97], v[240:243], v[144:147], v[82:97]
	s_waitcnt lgkmcnt(4)
	v_mfma_f32_32x32x16_bf16 v[66:81], v[244:247], v[144:147], v[66:81]
	ds_read_b128 v[240:243], v202 offset:24832
	ds_read_b128 v[244:247], v202 offset:37120
	s_waitcnt lgkmcnt(5)
	v_mfma_f32_32x32x16_bf16 v[82:97], v[212:215], v[140:143], v[82:97]
	v_add_f32_e32 v212, v149, v168
	v_mov_b32_e32 v213, v212
	v_cvt_pk_bf16_f32 v168, v169, v191
	v_cvt_pk_bf16_f32 v169, v170, v192
	v_cvt_pk_bf16_f32 v170, v190, v193
	v_cvt_pk_bf16_f32 v171, v171, v189
	v_cvt_pk_bf16_f32 v172, v173, v175
	s_waitcnt lgkmcnt(4)
	v_mfma_f32_32x32x16_bf16 v[66:81], v[216:219], v[140:143], v[66:81]
	v_cvt_pk_bf16_f32 v173, v174, v188
	v_cvt_pk_bf16_f32 v174, v164, v166
	v_permlane32_swap_b32_e32 v212, v213
	v_permlane32_swap_b32_e32 v168, v170
	v_cvt_pk_bf16_f32 v175, v165, v167
	s_waitcnt lgkmcnt(3)
	v_mfma_f32_32x32x16_bf16 v[82:97], v[230:233], v[136:139], v[82:97]
	v_permlane32_swap_b32_e32 v172, v174
	v_cvt_pk_bf16_f32 v214, v162, v163
	v_cvt_pk_bf16_f32 v215, v160, v161
	v_cvt_pk_bf16_f32 v216, v156, v157
	v_cvt_pk_bf16_f32 v217, v152, v153
	v_cvt_pk_bf16_f32 v230, v150, v151
	s_waitcnt lgkmcnt(2)
	v_mfma_f32_32x32x16_bf16 v[66:81], v[236:239], v[136:139], v[66:81]
	v_cvt_pk_bf16_f32 v231, v158, v159
	v_cvt_pk_bf16_f32 v232, v154, v155
	v_cvt_pk_bf16_f32 v233, v148, v149
	v_permlane32_swap_b32_e32 v169, v171
	v_permlane32_swap_b32_e32 v173, v175
	s_waitcnt lgkmcnt(1)
	v_mfma_f32_32x32x16_bf16 v[82:97], v[240:243], v[132:135], v[82:97]
	v_permlane32_swap_b32_e32 v214, v216
	v_permlane32_swap_b32_e32 v215, v217
	v_permlane32_swap_b32_e32 v230, v232
	v_permlane32_swap_b32_e32 v231, v233
	s_waitcnt lgkmcnt(0)
	v_mfma_f32_32x32x16_bf16 v[66:81], v[244:247], v[132:135], v[66:81]
	ds_read_b64_tr_b16 v[236:237], v200 offset:0
	ds_read_b64_tr_b16 v[238:239], v200 offset:0x800
	ds_read_b64_tr_b16 v[240:241], v200 offset:0x1000
	ds_read_b64_tr_b16 v[242:243], v200 offset:0x1800
	ds_read_b64_tr_b16 v[244:245], v200 offset:0x2000
	ds_read_b64_tr_b16 v[246:247], v200 offset:0x2800
	ds_read_b64_tr_b16 v[222:223], v200 offset:0x3000
	ds_read_b64_tr_b16 v[224:225], v200 offset:0x3800
	s_waitcnt lgkmcnt(0)
	s_nop 0
	v_mfma_f32_32x32x16_bf16 v[2:17], v[168:171], v[236:239], v[2:17]
	v_readfirstlane_b32 s4, v0
	s_nop 0
	s_lshl_b32 s5, s4, 4
	s_mul_i32 s4, s5, 3
	s_add_i32 m0, s4, 0x8000
	s_nop 0
	global_load_lds_dwordx4 v[182:183], off
	v_mfma_f32_32x32x16_bf16 v[2:17], v[172:175], v[240:243], v[2:17]
	s_add_i32 m0, s4, 0x8400
	s_nop 0
	global_load_lds_dwordx4 v[184:185], off
	v_mfma_f32_32x32x16_bf16 v[2:17], v[214:217], v[244:247], v[2:17]
	s_add_i32 m0, s4, 0x8800
	s_nop 0
	global_load_lds_dwordx4 v[186:187], off
	v_mfma_f32_32x32x16_bf16 v[2:17], v[230:233], v[222:225], v[2:17]
	s_lshl_b32 s5, s5, 1
	s_add_i32 m0, s5, 0x4000
	s_nop 0
	global_load_lds_dwordx4 v[206:207], off
	ds_read_b64_tr_b16 v[222:223], v200 offset:0x200
	ds_read_b64_tr_b16 v[224:225], v200 offset:0xa00
	ds_read_b64_tr_b16 v[236:237], v200 offset:0x1200
	ds_read_b64_tr_b16 v[238:239], v200 offset:0x1a00
	ds_read_b64_tr_b16 v[240:241], v200 offset:0x2200
	ds_read_b64_tr_b16 v[242:243], v200 offset:0x2a00
	ds_read_b64_tr_b16 v[244:245], v200 offset:0x3200
	ds_read_b64_tr_b16 v[246:247], v200 offset:0x3a00
	s_waitcnt lgkmcnt(0)
	s_nop 0
	v_mfma_f32_32x32x16_bf16 v[50:65], v[168:171], v[222:225], v[50:65]
	s_add_i32 m0, s5, 0x4380
	s_nop 0
	global_load_lds_dwordx4 v[206:207], off offset:128
	ds_read_b64_tr_b16 v[222:223], v200 offset:0x400
	ds_read_b64_tr_b16 v[224:225], v200 offset:0xc00
	v_mfma_f32_32x32x16_bf16 v[50:65], v[172:175], v[236:239], v[50:65]
	v_add_co_u32_e32 v182, vcc, v182, v205
	s_nop 1
	v_addc_co_u32_e32 v183, vcc, 0, v183, vcc
	v_add_co_u32_e32 v184, vcc, v184, v208
	s_nop 1
	v_addc_co_u32_e32 v185, vcc, 0, v185, vcc
	v_add_co_u32_e32 v186, vcc, v186, v209
	s_nop 1
	v_addc_co_u32_e32 v187, vcc, 0, v187, vcc
	ds_read_b64_tr_b16 v[236:237], v200 offset:0x1400
	ds_read_b64_tr_b16 v[238:239], v200 offset:0x1c00
	v_mfma_f32_32x32x16_bf16 v[50:65], v[214:217], v[240:243], v[50:65]
	v_add_co_u32_e32 v206, vcc, 0x38000, v206
	s_nop 1
	v_addc_co_u32_e32 v207, vcc, 0, v207, vcc
	ds_read_b64_tr_b16 v[240:241], v200 offset:0x2400
	ds_read_b64_tr_b16 v[242:243], v200 offset:0x2c00
	v_mfma_f32_32x32x16_bf16 v[50:65], v[230:233], v[244:247], v[50:65]
	ds_read_b64_tr_b16 v[244:245], v200 offset:0x3400
	ds_read_b64_tr_b16 v[246:247], v200 offset:0x3c00
	s_waitcnt lgkmcnt(0)
	v_mfma_f32_32x32x16_bf16 v[34:49], v[168:171], v[222:225], v[34:49]
	ds_read_b64_tr_b16 v[222:223], v200 offset:0x600
	ds_read_b64_tr_b16 v[224:225], v200 offset:0xe00
	v_mfma_f32_32x32x16_bf16 v[34:49], v[172:175], v[236:239], v[34:49]
	ds_read_b64_tr_b16 v[236:237], v200 offset:0x1600
	ds_read_b64_tr_b16 v[238:239], v200 offset:0x1e00
	v_mfma_f32_32x32x16_bf16 v[34:49], v[214:217], v[240:243], v[34:49]
	ds_read_b64_tr_b16 v[240:241], v200 offset:0x2600
	ds_read_b64_tr_b16 v[242:243], v200 offset:0x2e00
	v_mfma_f32_32x32x16_bf16 v[34:49], v[230:233], v[244:247], v[34:49]
	ds_read_b64_tr_b16 v[244:245], v200 offset:0x3600
	ds_read_b64_tr_b16 v[246:247], v200 offset:0x3e00
	s_waitcnt lgkmcnt(0)
	v_mfma_f32_32x32x16_bf16 v[18:33], v[168:171], v[222:225], v[18:33]
	v_max_f32_e32 v168, v83, v83
	v_max_f32_e32 v169, v82, v82
	v_max_f32_e32 v168, v169, v168
	v_max3_f32 v168, v168, v84, v85
	v_max3_f32 v168, v168, v86, v87
	v_max3_f32 v168, v168, v88, v89
	v_max3_f32 v168, v168, v90, v91
	v_max3_f32 v168, v168, v92, v93
	v_max3_f32 v168, v168, v94, v95
	v_mfma_f32_32x32x16_bf16 v[18:33], v[172:175], v[236:239], v[18:33]
	v_max3_f32 v168, v168, v96, v97
	v_max3_f32 v168, v168, v66, v67
	v_max3_f32 v168, v168, v68, v69
	v_max3_f32 v168, v168, v70, v71
	v_max3_f32 v168, v168, v72, v73
	v_max3_f32 v168, v168, v74, v75
	v_max3_f32 v168, v168, v76, v77
	v_max3_f32 v168, v168, v78, v79
	v_mfma_f32_32x32x16_bf16 v[18:33], v[214:217], v[240:243], v[18:33]
	v_max3_f32 v168, v168, v80, v81
	v_mov_b32_e32 v169, v168
	s_nop 1
	v_permlane32_swap_b32_e32 v168, v169
	v_max_f32_e32 v169, v169, v169
	v_max_f32_e32 v168, v168, v168
	v_max_f32_e32 v168, v168, v169
	v_sub_f32_e32 v169, v168, v211
	v_cmp_ge_f32_e32 vcc, s11, v169
	v_max_f32_e32 v169, v211, v211
	v_max_f32_e32 v168, v169, v168
	v_mfma_f32_32x32x16_bf16 v[18:33], v[230:233], v[244:247], v[18:33]
	v_sub_f32_e32 v169, v211, v168
	v_mul_f32_e32 v169, 0x3dd53b94, v169
	v_exp_f32_e32 v169, v169
	s_cmp_eq_u64 vcc, exec
	s_cselect_b64 s[18:19], -1, 0
	v_cndmask_b32_e64 v172, v169, 1.0, s[18:19]
	v_cmp_gt_f32_e32 vcc, 1.0, v172
	s_cbranch_vccz .LBB0_1348
	s_and_saveexec_b64 s[4:5], s[0:1]
	ds_write_b32 v197, v172 offset:128
	s_or_b64 exec, exec, s[4:5]
	s_waitcnt lgkmcnt(0)
	v_add_u32_e32 v160, v196, v98
	ds_read_b128 v[148:151], v160 offset:224
	ds_read_b128 v[152:155], v160 offset:192
	ds_read_b128 v[156:159], v160 offset:160
	ds_read_b128 v[160:163], v160 offset:128
	v_mov_b32_e32 v228, 0xffffce00
	s_waitcnt lgkmcnt(3)
	v_pk_mul_f32 v[14:15], v[14:15], v[148:149]
	s_waitcnt lgkmcnt(2)
	v_pk_mul_f32 v[10:11], v[10:11], v[152:153]
	s_waitcnt lgkmcnt(1)
	v_pk_mul_f32 v[6:7], v[6:7], v[156:157]
	v_pk_mul_f32 v[16:17], v[16:17], v[150:151]
	v_pk_mul_f32 v[12:13], v[12:13], v[154:155]
	v_pk_mul_f32 v[8:9], v[8:9], v[158:159]
	s_waitcnt lgkmcnt(0)
	v_pk_mul_f32 v[4:5], v[4:5], v[162:163]
	v_pk_mul_f32 v[2:3], v[2:3], v[160:161]
	v_pk_mul_f32 v[62:63], v[62:63], v[148:149]
	v_pk_mul_f32 v[58:59], v[58:59], v[152:153]
	v_pk_mul_f32 v[54:55], v[54:55], v[156:157]
	v_pk_mul_f32 v[64:65], v[64:65], v[150:151]
	v_pk_mul_f32 v[60:61], v[60:61], v[154:155]
	v_pk_mul_f32 v[56:57], v[56:57], v[158:159]
	v_pk_mul_f32 v[52:53], v[52:53], v[162:163]
	v_pk_mul_f32 v[50:51], v[50:51], v[160:161]
	v_pk_mul_f32 v[46:47], v[46:47], v[148:149]
	v_pk_mul_f32 v[42:43], v[42:43], v[152:153]
	v_pk_mul_f32 v[38:39], v[38:39], v[156:157]
	v_pk_mul_f32 v[48:49], v[48:49], v[150:151]
	v_pk_mul_f32 v[44:45], v[44:45], v[154:155]
	v_pk_mul_f32 v[40:41], v[40:41], v[158:159]
	v_pk_mul_f32 v[36:37], v[36:37], v[162:163]
	v_pk_mul_f32 v[34:35], v[34:35], v[160:161]
	v_pk_mul_f32 v[30:31], v[30:31], v[148:149]
	v_pk_mul_f32 v[26:27], v[26:27], v[152:153]
	v_pk_mul_f32 v[22:23], v[22:23], v[156:157]
	v_pk_mul_f32 v[32:33], v[32:33], v[150:151]
	v_pk_mul_f32 v[28:29], v[28:29], v[154:155]
	v_pk_mul_f32 v[24:25], v[24:25], v[158:159]
	v_pk_mul_f32 v[20:21], v[20:21], v[162:163]
	v_pk_mul_f32 v[18:19], v[18:19], v[160:161]
	s_branch .LBB0_1349

.LBB0_1349:
	v_cndmask_b32_e64 v173, v168, v211, s[18:19]
	v_mul_f32_e32 v164, 0xbdd53b94, v173
	v_fmamk_f32 v82, v82, 0x3dd53b94, v164
	v_fmamk_f32 v83, v83, 0x3dd53b94, v164
	v_fmamk_f32 v84, v84, 0x3dd53b94, v164
	v_fmamk_f32 v85, v85, 0x3dd53b94, v164
	v_fmamk_f32 v86, v86, 0x3dd53b94, v164
	v_fmamk_f32 v87, v87, 0x3dd53b94, v164
	v_fmamk_f32 v88, v88, 0x3dd53b94, v164
	v_fmamk_f32 v89, v89, 0x3dd53b94, v164
	v_fmamk_f32 v90, v90, 0x3dd53b94, v164
	v_fmamk_f32 v91, v91, 0x3dd53b94, v164
	v_fmamk_f32 v92, v92, 0x3dd53b94, v164
	v_fmamk_f32 v93, v93, 0x3dd53b94, v164
	v_fmamk_f32 v94, v94, 0x3dd53b94, v164
	v_fmamk_f32 v95, v95, 0x3dd53b94, v164
	v_fmamk_f32 v96, v96, 0x3dd53b94, v164
	v_fmamk_f32 v97, v97, 0x3dd53b94, v164
	v_fmamk_f32 v229, v68, 0x3dd53b94, v164
	v_fmamk_f32 v230, v69, 0x3dd53b94, v164
	v_fmamk_f32 v168, v73, 0x3dd53b94, v164
	v_fmamk_f32 v169, v74, 0x3dd53b94, v164
	v_fmamk_f32 v175, v66, 0x3dd53b94, v164
	v_fmamk_f32 v211, v67, 0x3dd53b94, v164
	v_fmamk_f32 v231, v70, 0x3dd53b94, v164
	v_fmamk_f32 v166, v71, 0x3dd53b94, v164
	v_fmamk_f32 v167, v72, 0x3dd53b94, v164
	v_fmamk_f32 v170, v75, 0x3dd53b94, v164
	v_fmamk_f32 v171, v76, 0x3dd53b94, v164
	v_fmamk_f32 v174, v77, 0x3dd53b94, v164
	v_fmamk_f32 v165, v78, 0x3dd53b94, v164
	v_exp_f32_e32 v161, v82
	v_exp_f32_e32 v163, v83
	v_exp_f32_e32 v159, v84
	v_exp_f32_e32 v162, v85
	v_exp_f32_e32 v158, v86
	v_exp_f32_e32 v160, v87
	v_exp_f32_e32 v156, v88
	v_exp_f32_e32 v157, v89
	v_exp_f32_e32 v153, v90
	v_exp_f32_e32 v155, v91
	v_exp_f32_e32 v152, v92
	v_exp_f32_e32 v154, v93
	v_exp_f32_e32 v149, v94
	v_exp_f32_e32 v151, v95
	v_exp_f32_e32 v148, v96
	v_exp_f32_e32 v150, v97
	v_fmamk_f32 v232, v79, 0x3dd53b94, v164
	v_fmamk_f32 v233, v80, 0x3dd53b94, v164
	v_fmac_f32_e32 v164, 0x3dd53b94, v81
	s_waitcnt vmcnt(0) lgkmcnt(0)
	s_barrier
	ds_read_b128 v[214:217], v203
	ds_read_b128 v[222:225], v203 offset:12288
	ds_read_b128 v[236:239], v204
	ds_read_b128 v[240:243], v204 offset:12288
	ds_read_b128 v[66:69], v201 offset:12288
	ds_read_b128 v[70:73], v201
	ds_read_b128 v[244:247], v202
	ds_read_b128 v[176:179], v202 offset:12288
	v_exp_f32_e32 v166, v166
	v_exp_f32_e32 v167, v167
	v_exp_f32_e32 v218, v169
	s_waitcnt lgkmcnt(2)
	v_mfma_f32_32x32x16_bf16 v[82:97], v[70:73], v[128:131], 0
	v_exp_f32_e32 v219, v170
	v_exp_f32_e32 v165, v165
	v_exp_f32_e32 v164, v164
	v_mfma_f32_32x32x16_bf16 v[82:97], v[214:217], v[124:127], v[82:97]
	v_mfma_f32_32x32x16_bf16 v[82:97], v[236:239], v[120:123], v[82:97]
	v_mfma_f32_32x32x16_bf16 v[66:81], v[66:69], v[128:131], 0
	s_waitcnt lgkmcnt(1)
	v_mfma_f32_32x32x16_bf16 v[82:97], v[244:247], v[116:119], v[82:97]
	v_mfma_f32_32x32x16_bf16 v[66:81], v[222:225], v[124:127], v[66:81]
	ds_read_b128 v[214:217], v201 offset:128
	ds_read_b128 v[222:225], v201 offset:12416
	s_waitcnt lgkmcnt(1)
	v_mfma_f32_32x32x16_bf16 v[82:97], v[214:217], v[112:115], v[82:97]
	v_mfma_f32_32x32x16_bf16 v[66:81], v[240:243], v[120:123], v[66:81]
	ds_read_b128 v[236:239], v203 offset:128
	ds_read_b128 v[240:243], v203 offset:12416
	s_waitcnt lgkmcnt(1)
	v_mfma_f32_32x32x16_bf16 v[82:97], v[236:239], v[108:111], v[82:97]
	v_mfma_f32_32x32x16_bf16 v[66:81], v[176:179], v[116:119], v[66:81]
	ds_read_b128 v[176:179], v204 offset:128
	ds_read_b128 v[244:247], v204 offset:12416
	s_waitcnt lgkmcnt(1)
	v_mfma_f32_32x32x16_bf16 v[82:97], v[176:179], v[104:107], v[82:97]
	v_mfma_f32_32x32x16_bf16 v[66:81], v[222:225], v[112:115], v[66:81]
	ds_read_b128 v[214:217], v202 offset:128
	ds_read_b128 v[222:225], v202 offset:12416
	s_waitcnt lgkmcnt(1)
	v_mfma_f32_32x32x16_bf16 v[82:97], v[214:217], v[100:103], v[82:97]
	v_mfma_f32_32x32x16_bf16 v[66:81], v[240:243], v[108:111], v[66:81]
	ds_read_b128 v[236:239], v201 offset:256
	ds_read_b128 v[240:243], v201 offset:12544
	s_waitcnt lgkmcnt(1)
	v_mfma_f32_32x32x16_bf16 v[82:97], v[236:239], v[144:147], v[82:97]
	v_mfma_f32_32x32x16_bf16 v[66:81], v[244:247], v[104:107], v[66:81]
	ds_read_b128 v[176:179], v203 offset:256
	ds_read_b128 v[244:247], v203 offset:12544
	s_waitcnt lgkmcnt(1)
	v_mfma_f32_32x32x16_bf16 v[82:97], v[176:179], v[140:143], v[82:97]
	v_exp_f32_e32 v178, v175
	v_exp_f32_e32 v179, v211
	v_exp_f32_e32 v211, v229
	v_mfma_f32_32x32x16_bf16 v[66:81], v[222:225], v[100:103], v[66:81]
	ds_read_b128 v[214:217], v204 offset:256
	ds_read_b128 v[222:225], v204 offset:12544
	s_waitcnt lgkmcnt(1)
	v_mfma_f32_32x32x16_bf16 v[82:97], v[214:217], v[136:139], v[82:97]
	v_exp_f32_e32 v217, v168
	v_add_f32_e32 v168, 0, v161
	v_add_f32_e32 v168, v163, v168
	v_add_f32_e32 v168, v159, v168
	v_add_f32_e32 v168, v162, v168
	v_add_f32_e32 v168, v158, v168
	v_add_f32_e32 v168, v160, v168
	v_mfma_f32_32x32x16_bf16 v[66:81], v[240:243], v[144:147], v[66:81]
	v_add_f32_e32 v168, v156, v168
	v_add_f32_e32 v168, v157, v168
	v_add_f32_e32 v168, v153, v168
	v_add_f32_e32 v168, v155, v168
	v_add_f32_e32 v168, v152, v168
	v_add_f32_e32 v168, v154, v168
	v_add_f32_e32 v168, v149, v168
	v_mfma_f32_32x32x16_bf16 v[66:81], v[244:247], v[140:143], v[66:81]
	v_add_f32_e32 v168, v151, v168
	v_add_f32_e32 v168, v148, v168
	v_exp_f32_e32 v215, v230
	v_add_f32_e32 v168, v150, v168
	v_exp_f32_e32 v216, v231
	v_add_f32_e32 v168, v178, v168
	v_add_f32_e32 v168, v179, v168
	s_waitcnt lgkmcnt(0)
	v_mfma_f32_32x32x16_bf16 v[66:81], v[222:225], v[136:139], v[66:81]
	v_add_f32_e32 v168, v211, v168
	v_add_f32_e32 v168, v215, v168
	v_add_f32_e32 v168, v216, v168
	ds_read_b128 v[236:239], v202 offset:256
	ds_read_b128 v[240:243], v202 offset:12544
	v_add_f32_e32 v168, v166, v168
	v_exp_f32_e32 v223, v171
	v_add_f32_e32 v168, v167, v168
	v_exp_f32_e32 v224, v174
	v_add_f32_e32 v168, v217, v168
	v_add_f32_e32 v168, v218, v168
	v_exp_f32_e32 v225, v232
	v_add_f32_e32 v168, v219, v168
	s_waitcnt lgkmcnt(1)
	v_mfma_f32_32x32x16_bf16 v[82:97], v[236:239], v[132:135], v[82:97]
	v_exp_f32_e32 v231, v233
	v_add_f32_e32 v168, v223, v168
	v_add_f32_e32 v168, v224, v168
	v_add_f32_e32 v168, v165, v168
	v_add_f32_e32 v168, v225, v168
	v_add_f32_e32 v168, v231, v168
	v_add_f32_e32 v229, v164, v168
	s_waitcnt lgkmcnt(0)
	v_mfma_f32_32x32x16_bf16 v[66:81], v[240:243], v[132:135], v[66:81]
	v_mov_b32_e32 v230, v229
	v_cvt_pk_bf16_f32 v168, v161, v163
	v_cvt_pk_bf16_f32 v169, v159, v162
	v_cvt_pk_bf16_f32 v170, v158, v160
	v_cvt_pk_bf16_f32 v171, v156, v157
	s_nop 1
	v_permlane32_swap_b32_e32 v229, v230
	v_permlane32_swap_b32_e32 v168, v170
	v_permlane32_swap_b32_e32 v169, v171
	v_cvt_pk_bf16_f32 v174, v153, v155
	v_cvt_pk_bf16_f32 v175, v152, v154
	v_cvt_pk_bf16_f32 v176, v149, v151
	v_cvt_pk_bf16_f32 v177, v148, v150
	v_cvt_pk_bf16_f32 v214, v178, v179
	v_cvt_pk_bf16_f32 v215, v211, v215
	v_cvt_pk_bf16_f32 v216, v216, v166
	v_cvt_pk_bf16_f32 v217, v167, v217
	v_cvt_pk_bf16_f32 v222, v218, v219
	v_cvt_pk_bf16_f32 v223, v223, v224
	v_cvt_pk_bf16_f32 v224, v165, v225
	v_cvt_pk_bf16_f32 v225, v231, v164
	s_nop 0
	v_permlane32_swap_b32_e32 v174, v176
	v_permlane32_swap_b32_e32 v175, v177
	v_permlane32_swap_b32_e32 v214, v216
	v_permlane32_swap_b32_e32 v215, v217
	v_permlane32_swap_b32_e32 v222, v224
	v_permlane32_swap_b32_e32 v223, v225
	ds_read_b64_tr_b16 v[188:189], v198 offset:0
	ds_read_b64_tr_b16 v[190:191], v198 offset:0x800
	ds_read_b64_tr_b16 v[236:237], v198 offset:0x1000
	ds_read_b64_tr_b16 v[238:239], v198 offset:0x1800
	ds_read_b64_tr_b16 v[240:241], v198 offset:0x2000
	ds_read_b64_tr_b16 v[242:243], v198 offset:0x2800
	ds_read_b64_tr_b16 v[244:245], v198 offset:0x3000
	ds_read_b64_tr_b16 v[246:247], v198 offset:0x3800
	s_waitcnt lgkmcnt(0)
	s_nop 0
	v_mfma_f32_32x32x16_bf16 v[2:17], v[168:171], v[188:191], v[2:17]
	v_readfirstlane_b32 s4, v0
	s_nop 0
	s_lshl_b32 s5, s4, 4
	s_mul_i32 s4, s5, 3
	s_add_i32 m0, s4, 0xe000
	s_nop 0
	global_load_lds_dwordx4 v[182:183], off
	ds_read_b64_tr_b16 v[188:189], v198 offset:0x200
	ds_read_b64_tr_b16 v[190:191], v198 offset:0xa00
	v_mfma_f32_32x32x16_bf16 v[2:17], v[174:177], v[236:239], v[2:17]
	s_add_i32 m0, s4, 0xe400
	s_nop 0
	global_load_lds_dwordx4 v[184:185], off
	ds_read_b64_tr_b16 v[236:237], v198 offset:0x1200
	ds_read_b64_tr_b16 v[238:239], v198 offset:0x1a00
	v_mfma_f32_32x32x16_bf16 v[2:17], v[214:217], v[240:243], v[2:17]
	s_add_i32 m0, s4, 0xe800
	s_nop 0
	global_load_lds_dwordx4 v[186:187], off
	ds_read_b64_tr_b16 v[240:241], v198 offset:0x2200
	ds_read_b64_tr_b16 v[242:243], v198 offset:0x2a00
	v_mfma_f32_32x32x16_bf16 v[2:17], v[222:225], v[244:247], v[2:17]
	s_lshl_b32 s5, s5, 1
	s_mov_b32 m0, s5
	s_nop 0
	global_load_lds_dwordx4 v[206:207], off
	ds_read_b64_tr_b16 v[244:245], v198 offset:0x3200
	ds_read_b64_tr_b16 v[246:247], v198 offset:0x3a00
	s_waitcnt lgkmcnt(0)
	v_mfma_f32_32x32x16_bf16 v[50:65], v[168:171], v[188:191], v[50:65]
	s_add_i32 m0, s5, 0x380
	s_nop 0
	global_load_lds_dwordx4 v[206:207], off offset:128
	ds_read_b64_tr_b16 v[188:189], v198 offset:0x400
	ds_read_b64_tr_b16 v[190:191], v198 offset:0xc00
	v_mfma_f32_32x32x16_bf16 v[50:65], v[174:177], v[236:239], v[50:65]
	v_add_co_u32_e32 v182, vcc, v182, v205
	s_nop 1
	v_addc_co_u32_e32 v183, vcc, 0, v183, vcc
	v_add_co_u32_e32 v184, vcc, v184, v208
	s_nop 1
	v_addc_co_u32_e32 v185, vcc, 0, v185, vcc
	v_add_co_u32_e32 v186, vcc, v186, v209
	s_nop 1
	v_addc_co_u32_e32 v187, vcc, 0, v187, vcc
	ds_read_b64_tr_b16 v[236:237], v198 offset:0x1400
	ds_read_b64_tr_b16 v[238:239], v198 offset:0x1c00
	v_mfma_f32_32x32x16_bf16 v[50:65], v[214:217], v[240:243], v[50:65]
	v_add_co_u32_e32 v206, vcc, 0x38000, v206
	s_nop 1
	v_addc_co_u32_e32 v207, vcc, 0, v207, vcc
	ds_read_b64_tr_b16 v[240:241], v198 offset:0x2400
	ds_read_b64_tr_b16 v[242:243], v198 offset:0x2c00
	v_mfma_f32_32x32x16_bf16 v[50:65], v[222:225], v[244:247], v[50:65]
	ds_read_b64_tr_b16 v[244:245], v198 offset:0x3400
	ds_read_b64_tr_b16 v[246:247], v198 offset:0x3c00
	s_waitcnt lgkmcnt(0)
	v_mfma_f32_32x32x16_bf16 v[34:49], v[168:171], v[188:191], v[34:49]
	ds_read_b64_tr_b16 v[188:189], v198 offset:0x600
	ds_read_b64_tr_b16 v[190:191], v198 offset:0xe00
	v_mfma_f32_32x32x16_bf16 v[34:49], v[174:177], v[236:239], v[34:49]
	ds_read_b64_tr_b16 v[236:237], v198 offset:0x1600
	ds_read_b64_tr_b16 v[238:239], v198 offset:0x1e00
	v_mfma_f32_32x32x16_bf16 v[34:49], v[214:217], v[240:243], v[34:49]
	ds_read_b64_tr_b16 v[240:241], v198 offset:0x2600
	ds_read_b64_tr_b16 v[242:243], v198 offset:0x2e00
	v_mfma_f32_32x32x16_bf16 v[34:49], v[222:225], v[244:247], v[34:49]
	ds_read_b64_tr_b16 v[244:245], v198 offset:0x3600
	ds_read_b64_tr_b16 v[246:247], v198 offset:0x3e00
	s_waitcnt lgkmcnt(0)
	v_mfma_f32_32x32x16_bf16 v[18:33], v[168:171], v[188:191], v[18:33]
	v_max_f32_e32 v168, v83, v83
	v_max_f32_e32 v169, v82, v82
	v_max_f32_e32 v168, v169, v168
	v_max3_f32 v168, v168, v84, v85
	v_max3_f32 v168, v168, v86, v87
	v_max3_f32 v168, v168, v88, v89
	v_max3_f32 v168, v168, v90, v91
	v_max3_f32 v168, v168, v92, v93
	v_max3_f32 v168, v168, v94, v95
	v_mfma_f32_32x32x16_bf16 v[18:33], v[174:177], v[236:239], v[18:33]
	v_max3_f32 v168, v168, v96, v97
	v_max3_f32 v168, v168, v66, v67
	v_max3_f32 v168, v168, v68, v69
	v_max3_f32 v168, v168, v70, v71
	v_max3_f32 v168, v168, v72, v73
	v_max3_f32 v168, v168, v74, v75
	v_max3_f32 v168, v168, v76, v77
	v_max3_f32 v168, v168, v78, v79
	v_mfma_f32_32x32x16_bf16 v[18:33], v[214:217], v[240:243], v[18:33]
	v_max3_f32 v168, v168, v80, v81
	v_mov_b32_e32 v169, v168
	s_nop 1
	v_permlane32_swap_b32_e32 v168, v169
	v_max_f32_e32 v169, v169, v169
	v_max_f32_e32 v168, v168, v168
	v_max_f32_e32 v168, v168, v169
	v_sub_f32_e32 v169, v168, v173
	v_cmp_ge_f32_e32 vcc, s11, v169
	v_max_f32_e32 v169, v173, v173
	v_max_f32_e32 v169, v169, v168
	v_mfma_f32_32x32x16_bf16 v[18:33], v[222:225], v[244:247], v[18:33]
	v_sub_f32_e32 v168, v173, v169
	v_mul_f32_e32 v168, 0x3dd53b94, v168
	v_exp_f32_e32 v168, v168
	s_cmp_eq_u64 vcc, exec
	s_cselect_b64 s[18:19], -1, 0
	v_cndmask_b32_e64 v168, v168, 1.0, s[18:19]
	v_cmp_gt_f32_e32 vcc, 1.0, v168
	s_cbranch_vccz .LBB0_1353
	s_mov_b64 s[4:5], exec
	s_and_b64 s[22:23], s[4:5], s[0:1]
	v_mov_b32_e32 v246, v227
	s_mov_b64 exec, s[22:23]
	ds_write_b32 v197, v168 offset:128
	s_or_b64 exec, exec, s[4:5]
	s_waitcnt lgkmcnt(0)
	v_add_u32_e32 v160, v196, v98
	ds_read_b128 v[148:151], v160 offset:224
	ds_read_b128 v[152:155], v160 offset:192
	ds_read_b128 v[156:159], v160 offset:160
	ds_read_b128 v[160:163], v160 offset:128
	s_waitcnt lgkmcnt(3)
	v_pk_mul_f32 v[14:15], v[14:15], v[148:149]
	s_waitcnt lgkmcnt(2)
	v_pk_mul_f32 v[10:11], v[10:11], v[152:153]
	s_waitcnt lgkmcnt(1)
	v_pk_mul_f32 v[6:7], v[6:7], v[156:157]
	v_pk_mul_f32 v[16:17], v[16:17], v[150:151]
	v_pk_mul_f32 v[12:13], v[12:13], v[154:155]
	v_pk_mul_f32 v[8:9], v[8:9], v[158:159]
	s_waitcnt lgkmcnt(0)
	v_pk_mul_f32 v[4:5], v[4:5], v[162:163]
	v_pk_mul_f32 v[2:3], v[2:3], v[160:161]
	v_pk_mul_f32 v[62:63], v[62:63], v[148:149]
	v_pk_mul_f32 v[58:59], v[58:59], v[152:153]
	v_pk_mul_f32 v[54:55], v[54:55], v[156:157]
	v_pk_mul_f32 v[64:65], v[64:65], v[150:151]
	v_pk_mul_f32 v[60:61], v[60:61], v[154:155]
	v_pk_mul_f32 v[56:57], v[56:57], v[158:159]
	v_pk_mul_f32 v[52:53], v[52:53], v[162:163]
	v_pk_mul_f32 v[50:51], v[50:51], v[160:161]
	v_pk_mul_f32 v[46:47], v[46:47], v[148:149]
	v_pk_mul_f32 v[42:43], v[42:43], v[152:153]
	v_pk_mul_f32 v[38:39], v[38:39], v[156:157]
	v_pk_mul_f32 v[48:49], v[48:49], v[150:151]
	v_pk_mul_f32 v[44:45], v[44:45], v[154:155]
	v_pk_mul_f32 v[40:41], v[40:41], v[158:159]
	v_pk_mul_f32 v[36:37], v[36:37], v[162:163]
	v_pk_mul_f32 v[34:35], v[34:35], v[160:161]
	v_pk_mul_f32 v[30:31], v[30:31], v[148:149]
	v_pk_mul_f32 v[26:27], v[26:27], v[152:153]
	v_pk_mul_f32 v[22:23], v[22:23], v[156:157]
	v_pk_mul_f32 v[32:33], v[32:33], v[150:151]
	v_pk_mul_f32 v[28:29], v[28:29], v[154:155]
	v_pk_mul_f32 v[24:25], v[24:25], v[158:159]
	v_pk_mul_f32 v[20:21], v[20:21], v[162:163]
	v_pk_mul_f32 v[18:19], v[18:19], v[160:161]
	s_branch .LBB0_1354
